# best2 + early L2 write-back in the grid barrier: the first workgroup of each XCD to arrive issues buffer_wbl2 before it starts polling
# baseline (speedup 1.0000x reference)
; DI unsigned xb_ld(unsigned* p)              { return __hip_atomic_load(p, __ATOMIC_RELAXED, __HIP_MEMORY_SCOPE_AGENT); }
; DI unsigned xb_add(unsigned* p, unsigned v) { return __hip_atomic_fetch_add(p, v, __ATOMIC_RELAXED, __HIP_MEMORY_SCOPE_AGENT); }
; #define XB_SPIN(cond, bar) do { unsigned _sp = 0; while (cond) { __builtin_amdgcn_s_sleep(1); \
;     if ((++_sp & 255u) == 0u) { if (xb_ld(&(bar)[XB_TMO])) break; if (_sp > XB_SPIN_CAP) { atomicAdd(&(bar)[XB_TMO], 1u); break; } } } } while (0)
; DI void xcd_barrier(const XcdBarrier& b) {
;     ...
;         const unsigned old = xb_add(&bar[XB_XSUB(b.x)], 1u);
;         const unsigned gen = old / nloc;
;         if (old + 1u == (gen + 1u) * nloc) {
;             __builtin_amdgcn_fence(__ATOMIC_RELEASE, "agent");
;             asm volatile("s_waitcnt vmcnt(0)" ::: "memory");
;             const unsigned og = xb_add(&bar[XB_TOP], 1u);
;             const unsigned tg = og / nx;
;             if (og + 1u == (tg + 1u) * nx) xb_add(&bar[XB_TOPGEN], 1u);
;             else XB_SPIN(xb_ld(&bar[XB_TOPGEN]) == tg, bar);
;             __builtin_amdgcn_fence(__ATOMIC_ACQUIRE, "agent");
;             xb_add(&bar[XB_XGEN(b.x)], 1u);
;             asm volatile("s_waitcnt vmcnt(0)" ::: "memory");
;         } else {
;             XB_SPIN(xb_ld(&bar[XB_XGEN(b.x)]) == gen, bar);
;             __builtin_amdgcn_fence(__ATOMIC_ACQUIRE, "agent");
.LBB0_65:
	s_or_b64 exec, exec, s[8:9]
	v_cvt_f32_u32_e32 v5, v3
	s_waitcnt vmcnt(0)
	v_readfirstlane_b32 s0, v4
	v_sub_u32_e32 v4, 0, v3
	v_rcp_iflag_f32_e32 v5, v5
	v_add_u32_e32 v6, s0, v2
	v_mul_f32_e32 v5, 0x4f7ffffe, v5
	v_cvt_u32_f32_e32 v5, v5
	v_mul_lo_u32 v2, v4, v5
	v_mul_hi_u32 v2, v5, v2
	v_add_u32_e32 v2, v5, v2
	v_mul_hi_u32 v2, v6, v2
	v_mul_lo_u32 v4, v2, v3
	v_sub_u32_e32 v4, v6, v4
	v_add_u32_e32 v5, 1, v2
	v_cmp_ge_u32_e32 vcc, v4, v3
	s_nop 1
	v_cndmask_b32_e32 v2, v2, v5, vcc
	v_sub_u32_e32 v5, v4, v3
	v_cndmask_b32_e32 v4, v4, v5, vcc
	v_add_u32_e32 v5, 1, v2
	v_cmp_ge_u32_e32 vcc, v4, v3
	v_add_u32_e32 v4, 1, v6
	s_nop 0
	v_cndmask_b32_e32 v2, v2, v5, vcc
	v_mul_lo_u32 v5, v3, v2
	v_add_u32_e32 v3, v5, v3
	v_cmp_ne_u32_e32 vcc, v4, v3
	s_and_saveexec_b64 s[0:1], vcc
	s_xor_b64 s[0:1], exec, s[0:1]
	s_cbranch_execz .LBB0_79
	v_sub_u32_e32 v1, v4, v5
	v_cmp_eq_u32_e32 vcc, 1, v1
	s_cbranch_vccz .Lpf_0
	buffer_wbl2 sc1
.Lpf_0:
	s_waitcnt lgkmcnt(0)
	v_mov_b32_e32 v1, 0x2000
	global_load_dword v1, v1, s[6:7] offset:1024 sc1
	s_add_u32 s12, s6, 0x2400
	s_addc_u32 s13, s7, 0
	s_waitcnt vmcnt(0)
	v_cmp_eq_u32_e32 vcc, v1, v2
	s_and_saveexec_b64 s[8:9], vcc
	s_cbranch_execz .LBB0_78
	s_add_u32 s10, s94, 0x4200
	s_addc_u32 s11, s95, 0
	s_mov_b32 s24, 1
	s_mov_b64 s[14:15], 0
	v_mov_b32_e32 v1, 0
	s_branch .LBB0_69

; DI unsigned xb_ld(unsigned* p)              { return __hip_atomic_load(p, __ATOMIC_RELAXED, __HIP_MEMORY_SCOPE_AGENT); }
; DI unsigned xb_add(unsigned* p, unsigned v) { return __hip_atomic_fetch_add(p, v, __ATOMIC_RELAXED, __HIP_MEMORY_SCOPE_AGENT); }
; #define XB_SPIN(cond, bar) do { unsigned _sp = 0; while (cond) { __builtin_amdgcn_s_sleep(1); \
;     if ((++_sp & 255u) == 0u) { if (xb_ld(&(bar)[XB_TMO])) break; if (_sp > XB_SPIN_CAP) { atomicAdd(&(bar)[XB_TMO], 1u); break; } } } } while (0)
; DI void xcd_barrier(const XcdBarrier& b) {
;     ...
;         const unsigned old = xb_add(&bar[XB_XSUB(b.x)], 1u);
;         const unsigned gen = old / nloc;
;         if (old + 1u == (gen + 1u) * nloc) {
;             __builtin_amdgcn_fence(__ATOMIC_RELEASE, "agent");
;             asm volatile("s_waitcnt vmcnt(0)" ::: "memory");
;             const unsigned og = xb_add(&bar[XB_TOP], 1u);
;             const unsigned tg = og / nx;
;             if (og + 1u == (tg + 1u) * nx) xb_add(&bar[XB_TOPGEN], 1u);
;             else XB_SPIN(xb_ld(&bar[XB_TOPGEN]) == tg, bar);
;             __builtin_amdgcn_fence(__ATOMIC_ACQUIRE, "agent");
;             xb_add(&bar[XB_XGEN(b.x)], 1u);
;             asm volatile("s_waitcnt vmcnt(0)" ::: "memory");
;         } else {
;             XB_SPIN(xb_ld(&bar[XB_XGEN(b.x)]) == gen, bar);
;             __builtin_amdgcn_fence(__ATOMIC_ACQUIRE, "agent");
.LBB0_310:
	s_or_b64 exec, exec, s[6:7]
	v_cvt_f32_u32_e32 v5, v3
	s_waitcnt vmcnt(0)
	v_readfirstlane_b32 s0, v4
	v_sub_u32_e32 v4, 0, v3
	v_rcp_iflag_f32_e32 v5, v5
	v_add_u32_e32 v6, s0, v2
	v_mul_f32_e32 v5, 0x4f7ffffe, v5
	v_cvt_u32_f32_e32 v5, v5
	v_mul_lo_u32 v2, v4, v5
	v_mul_hi_u32 v2, v5, v2
	v_add_u32_e32 v2, v5, v2
	v_mul_hi_u32 v2, v6, v2
	v_mul_lo_u32 v4, v2, v3
	v_sub_u32_e32 v4, v6, v4
	v_add_u32_e32 v5, 1, v2
	v_cmp_ge_u32_e32 vcc, v4, v3
	s_nop 1
	v_cndmask_b32_e32 v2, v2, v5, vcc
	v_sub_u32_e32 v5, v4, v3
	v_cndmask_b32_e32 v4, v4, v5, vcc
	v_add_u32_e32 v5, 1, v2
	v_cmp_ge_u32_e32 vcc, v4, v3
	v_add_u32_e32 v4, 1, v6
	s_nop 0
	v_cndmask_b32_e32 v2, v2, v5, vcc
	v_mul_lo_u32 v5, v3, v2
	v_add_u32_e32 v3, v5, v3
	v_cmp_ne_u32_e32 vcc, v4, v3
	s_and_saveexec_b64 s[0:1], vcc
	s_xor_b64 s[0:1], exec, s[0:1]
	s_cbranch_execz .LBB0_324
	v_sub_u32_e32 v1, v4, v5
	v_cmp_eq_u32_e32 vcc, 1, v1
	s_cbranch_vccz .Lpf_1
	buffer_wbl2 sc1
.Lpf_1:
	s_waitcnt lgkmcnt(0)
	v_mov_b32_e32 v1, 0x2000
	global_load_dword v1, v1, s[4:5] offset:1024 sc1
	s_add_u32 s10, s4, 0x2400
	s_addc_u32 s11, s5, 0
	s_waitcnt vmcnt(0)
	v_cmp_eq_u32_e32 vcc, v1, v2
	s_and_saveexec_b64 s[6:7], vcc
	s_cbranch_execz .LBB0_323
	s_add_u32 s8, s94, 0x4200
	s_addc_u32 s9, s95, 0
	s_mov_b32 s22, 1
	s_mov_b64 s[12:13], 0
	v_mov_b32_e32 v1, 0
	s_branch .LBB0_314

; DI unsigned xb_ld(unsigned* p)              { return __hip_atomic_load(p, __ATOMIC_RELAXED, __HIP_MEMORY_SCOPE_AGENT); }
; DI unsigned xb_add(unsigned* p, unsigned v) { return __hip_atomic_fetch_add(p, v, __ATOMIC_RELAXED, __HIP_MEMORY_SCOPE_AGENT); }
; #define XB_SPIN(cond, bar) do { unsigned _sp = 0; while (cond) { __builtin_amdgcn_s_sleep(1); \
;     if ((++_sp & 255u) == 0u) { if (xb_ld(&(bar)[XB_TMO])) break; if (_sp > XB_SPIN_CAP) { atomicAdd(&(bar)[XB_TMO], 1u); break; } } } } while (0)
; DI void xcd_barrier(const XcdBarrier& b) {
;     ...
;         const unsigned old = xb_add(&bar[XB_XSUB(b.x)], 1u);
;         const unsigned gen = old / nloc;
;         if (old + 1u == (gen + 1u) * nloc) {
;             __builtin_amdgcn_fence(__ATOMIC_RELEASE, "agent");
;             asm volatile("s_waitcnt vmcnt(0)" ::: "memory");
;             const unsigned og = xb_add(&bar[XB_TOP], 1u);
;             const unsigned tg = og / nx;
;             if (og + 1u == (tg + 1u) * nx) xb_add(&bar[XB_TOPGEN], 1u);
;             else XB_SPIN(xb_ld(&bar[XB_TOPGEN]) == tg, bar);
;             __builtin_amdgcn_fence(__ATOMIC_ACQUIRE, "agent");
;             xb_add(&bar[XB_XGEN(b.x)], 1u);
;             asm volatile("s_waitcnt vmcnt(0)" ::: "memory");
;         } else {
;             XB_SPIN(xb_ld(&bar[XB_XGEN(b.x)]) == gen, bar);
;             __builtin_amdgcn_fence(__ATOMIC_ACQUIRE, "agent");
.LBB0_1187:
	s_or_b64 exec, exec, s[8:9]
	v_cvt_f32_u32_e32 v4, v2
	s_waitcnt vmcnt(0)
	v_readfirstlane_b32 s6, v3
	v_sub_u32_e32 v3, 0, v2
	v_rcp_iflag_f32_e32 v4, v4
	v_add_u32_e32 v5, s6, v1
	v_mul_f32_e32 v4, 0x4f7ffffe, v4
	v_cvt_u32_f32_e32 v4, v4
	v_mul_lo_u32 v1, v3, v4
	v_mul_hi_u32 v1, v4, v1
	v_add_u32_e32 v1, v4, v1
	v_mul_hi_u32 v1, v5, v1
	v_mul_lo_u32 v3, v1, v2
	v_sub_u32_e32 v3, v5, v3
	v_add_u32_e32 v4, 1, v1
	v_cmp_ge_u32_e32 vcc, v3, v2
	s_nop 1
	v_cndmask_b32_e32 v1, v1, v4, vcc
	v_sub_u32_e32 v4, v3, v2
	v_cndmask_b32_e32 v3, v3, v4, vcc
	v_add_u32_e32 v4, 1, v1
	v_cmp_ge_u32_e32 vcc, v3, v2
	v_add_u32_e32 v3, 1, v5
	s_nop 0
	v_cndmask_b32_e32 v1, v1, v4, vcc
	v_mul_lo_u32 v4, v2, v1
	v_add_u32_e32 v2, v4, v2
	v_cmp_ne_u32_e32 vcc, v3, v2
	s_and_saveexec_b64 s[6:7], vcc
	s_xor_b64 s[6:7], exec, s[6:7]
	s_cbranch_execz .LBB0_1201
	v_sub_u32_e32 v0, v3, v4
	v_cmp_eq_u32_e32 vcc, 1, v0
	s_cbranch_vccz .Lpf_9
	buffer_wbl2 sc1
.Lpf_9:
	s_waitcnt lgkmcnt(0)
	v_mov_b32_e32 v0, 0x2000
	global_load_dword v0, v0, s[0:1] offset:1024 sc1
	s_add_u32 s12, s0, 0x2400
	s_addc_u32 s13, s1, 0
	s_waitcnt vmcnt(0)
	v_cmp_eq_u32_e32 vcc, v0, v1
	s_and_saveexec_b64 s[8:9], vcc
	s_cbranch_execz .LBB0_1200
	s_add_u32 s10, s94, 0x4200
	s_addc_u32 s11, s95, 0
	s_mov_b32 s24, 1
	s_mov_b64 s[14:15], 0
	v_mov_b32_e32 v0, 0
	s_branch .LBB0_1191
